# prep token-shift staging: cache-line pre-touch of the cur/prv row segments right after the first block loads (later serialized blocks hit in cache)
# baseline (speedup 1.0000x reference)
.LBB0_269:
	s_or_b64 exec, exec, s[4:5]
	v_mov_b32_e32 v0, s2
	v_mbcnt_lo_u32_b32 v104, -1, 0
	v_mbcnt_hi_u32_b32 v104, -1, v104
	v_readlane_b32 s0, v254, 0
	v_readfirstlane_b32 s62, v0
	v_mov_b32_e32 v0, 0
	v_add_u32_e32 v106, s0, v104
	v_readfirstlane_b32 s70, v0
	s_ashr_i32 s71, s70, 31
	s_waitcnt lgkmcnt(0)
	s_add_u32 s54, s60, s70
	s_addc_u32 s55, s61, s71
	s_add_u32 s58, s54, 0x37c80000
	s_addc_u32 s59, s55, 0
	s_lshl_b32 s33, s62, 5
	v_ashrrev_i32_e32 v109, 4, v106
	v_add_u32_e32 v8, s33, v109
	s_movk_i32 s0, 0x3400
	v_mov_b64_e32 v[0:1], s[58:59]
	v_mad_i64_i32 v[0:1], s[4:5], v8, s0, v[0:1]
	v_lshlrev_b32_e32 v176, 1, v104
	s_mov_b64 s[4:5], 0x1800
	v_and_b32_e32 v11, 30, v176
	v_lshl_add_u64 v[2:3], v[0:1], 0, s[4:5]
	v_lshlrev_b32_e32 v4, 1, v11
	v_lshl_add_u64 v[6:7], v[2:3], 0, v[4:5]
	global_load_dword v10, v[6:7], off
	global_load_dword v250, v[6:7], off offset:128
	global_load_dword v250, v[6:7], off offset:256
	global_load_dword v250, v[6:7], off offset:384
	global_load_dword v250, v[6:7], off offset:512
	v_writelane_b32 v254, s12, 18
	s_load_dwordx4 s[36:39], s[12:13], 0x30
	s_movk_i32 s4, 0xe400
	v_and_b32_e32 v6, 0x7ff, v8
	s_mov_b32 s5, -1
	v_cmp_ne_u32_e32 vcc, 0, v6
	v_lshl_add_u64 v[0:1], v[0:1], 0, s[4:5]
	v_writelane_b32 v254, s13, 19
	s_and_saveexec_b64 s[4:5], vcc
	s_cbranch_execz .LBB0_271
	v_mov_b32_e32 v5, 0
	v_lshl_add_u64 v[6:7], v[0:1], 0, v[4:5]
	global_load_dword v5, v[6:7], off
	global_load_dword v250, v[6:7], off offset:128
	global_load_dword v250, v[6:7], off offset:256
	global_load_dword v250, v[6:7], off offset:384
	global_load_dword v250, v[6:7], off offset:512

.LBB0_1361:
	s_or_b64 exec, exec, s[4:5]
	s_waitcnt lgkmcnt(0)
	v_mov_b32_e32 v0, s2
	v_readlane_b32 s0, v254, 0
	s_barrier
	v_mbcnt_lo_u32_b32 v104, -1, 0
	v_mbcnt_hi_u32_b32 v104, -1, v104
	s_movk_i32 s4, 0x3400
	v_add_u32_e32 v106, s0, v104
	v_readlane_b32 s0, v254, 18
	v_readfirstlane_b32 s78, v0
	v_mov_b32_e32 v0, 0
	v_readlane_b32 s1, v254, 19
	s_load_dwordx2 s[80:81], s[0:1], 0x188
	s_load_dwordx4 s[40:43], s[0:1], 0xd8
	v_readfirstlane_b32 s82, v0
	s_ashr_i32 s83, s82, 31
	v_ashrrev_i32_e32 v105, 4, v106
	s_waitcnt lgkmcnt(0)
	s_add_u32 s74, s80, s82
	s_addc_u32 s75, s81, s83
	s_add_u32 s0, s74, 0x37c80000
	s_addc_u32 s1, s75, 0
	s_lshl_b32 s33, s78, 5
	v_add_u32_e32 v9, s33, v105
	v_mov_b64_e32 v[0:1], s[0:1]
	v_mad_i64_i32 v[0:1], s[4:5], v9, s4, v[0:1]
	v_lshlrev_b32_e32 v176, 1, v104
	s_mov_b64 s[4:5], 0x1800
	v_and_b32_e32 v10, 30, v176
	v_mov_b32_e32 v5, 0
	v_lshl_add_u64 v[2:3], v[0:1], 0, s[4:5]
	v_lshlrev_b32_e32 v4, 1, v10
	v_lshl_add_u64 v[6:7], v[2:3], 0, v[4:5]
	global_load_dword v8, v[6:7], off
	global_load_dword v250, v[6:7], off offset:128
	global_load_dword v250, v[6:7], off offset:256
	global_load_dword v250, v[6:7], off offset:384
	global_load_dword v250, v[6:7], off offset:512
	s_movk_i32 s4, 0xe400
	v_and_b32_e32 v6, 0x7ff, v9
	s_mov_b32 s5, -1
	v_cmp_ne_u32_e32 vcc, 0, v6
	v_lshl_add_u64 v[0:1], v[0:1], 0, s[4:5]
	v_mov_b32_e32 v9, 0
	s_and_saveexec_b64 s[4:5], vcc
	s_cbranch_execz .LBB0_1363
	v_mov_b32_e32 v7, 0
	v_mov_b32_e32 v6, v4
	v_lshl_add_u64 v[6:7], v[0:1], 0, v[6:7]
	global_load_dword v9, v[6:7], off
	global_load_dword v250, v[6:7], off offset:128
	global_load_dword v250, v[6:7], off offset:256
	global_load_dword v250, v[6:7], off offset:384
	global_load_dword v250, v[6:7], off offset:512
